# loader: MoE weight tile conversion pipelined two iterations deep (no HBM latency inside a loader iteration); scanner pipelined across chunks
# speedup vs baseline: 1.0081x; 1.0081x over previous
.Lld_ldone_p2:
	s_waitcnt vmcnt(21)
	s_mov_b32 s88, 0xa800
	v_add_u32_e32 v83, s88, v7
	v_add_u32_e32 v96, s88, v8
	v_lshlrev_b32_e32 v92, 16, v118
	v_and_b32_e32 v93, s89, v118
	ds_write_b64 v96, v[92:93]
	v_lshlrev_b32_e32 v92, 16, v98
	v_and_b32_e32 v93, s89, v98
	v_mul_f32_e32 v84, 0x3fb8aa3b, v92
	v_mul_f32_e32 v85, 0x3fb8aa3b, v93
	v_lshlrev_b32_e32 v94, 16, v102
	v_and_b32_e32 v95, s89, v102
	ds_write_b64 v83, v[94:95] offset:0
	v_exp_f32_e64 v86, -v84
	v_exp_f32_e64 v87, -v85
	v_exp_f32_e32 v90, v84
	v_exp_f32_e32 v91, v85
	v_lshlrev_b32_e32 v92, 16, v106
	v_and_b32_e32 v93, s89, v106
	v_mul_f32_e32 v92, v92, v90
	v_mul_f32_e32 v93, v93, v91
	ds_write_b64 v83, v[92:93] offset:8192
	ds_write_b64 v83, v[86:87] offset:16384
	v_lshlrev_b32_e32 v94, 16, v110
	v_and_b32_e32 v95, s89, v110
	v_mul_f32_e32 v94, v94, v90
	v_mul_f32_e32 v95, v95, v91
	ds_write_b64 v83, v[94:95] offset:24576
	v_lshlrev_b32_e32 v92, 16, v114
	v_and_b32_e32 v93, s89, v114
	v_mul_f32_e32 v92, v92, v86
	v_mul_f32_e32 v93, v93, v87
	ds_write_b64 v83, v[92:93] offset:32768
	v_lshlrev_b32_e32 v92, 16, v99
	v_and_b32_e32 v93, s89, v99
	v_fmac_f32_e32 v84, 0x3fb8aa3b, v92
	v_fmac_f32_e32 v85, 0x3fb8aa3b, v93
	v_lshlrev_b32_e32 v94, 16, v103
	v_and_b32_e32 v95, s89, v103
	v_mul_f32_e32 v94, v94, v86
	v_mul_f32_e32 v95, v95, v87
	ds_write_b64 v83, v[94:95] offset:256
	v_exp_f32_e64 v88, -v84
	v_exp_f32_e64 v89, -v85
	v_exp_f32_e32 v90, v84
	v_exp_f32_e32 v91, v85
	v_lshlrev_b32_e32 v92, 16, v107
	v_and_b32_e32 v93, s89, v107
	v_mul_f32_e32 v92, v92, v90
	v_mul_f32_e32 v93, v93, v91
	ds_write_b64 v83, v[92:93] offset:8448
	ds_write_b64 v83, v[88:89] offset:16640
	v_lshlrev_b32_e32 v94, 16, v111
	v_and_b32_e32 v95, s89, v111
	v_mul_f32_e32 v94, v94, v90
	v_mul_f32_e32 v95, v95, v91
	ds_write_b64 v83, v[94:95] offset:24832
	v_lshlrev_b32_e32 v92, 16, v115
	v_and_b32_e32 v93, s89, v115
	v_mul_f32_e32 v92, v92, v88
	v_mul_f32_e32 v93, v93, v89
	ds_write_b64 v83, v[92:93] offset:33024
	v_lshlrev_b32_e32 v92, 16, v100
	v_and_b32_e32 v93, s89, v100
	v_fmac_f32_e32 v84, 0x3fb8aa3b, v92
	v_fmac_f32_e32 v85, 0x3fb8aa3b, v93
	v_lshlrev_b32_e32 v94, 16, v104
	v_and_b32_e32 v95, s89, v104
	v_mul_f32_e32 v94, v94, v88
	v_mul_f32_e32 v95, v95, v89
	ds_write_b64 v83, v[94:95] offset:512
	v_exp_f32_e64 v86, -v84
	v_exp_f32_e64 v87, -v85
	v_exp_f32_e32 v90, v84
	v_exp_f32_e32 v91, v85
	v_lshlrev_b32_e32 v92, 16, v108
	v_and_b32_e32 v93, s89, v108
	v_mul_f32_e32 v92, v92, v90
	v_mul_f32_e32 v93, v93, v91
	ds_write_b64 v83, v[92:93] offset:8704
	ds_write_b64 v83, v[86:87] offset:16896
	v_lshlrev_b32_e32 v94, 16, v112
	v_and_b32_e32 v95, s89, v112
	v_mul_f32_e32 v94, v94, v90
	v_mul_f32_e32 v95, v95, v91
	ds_write_b64 v83, v[94:95] offset:25088
	v_lshlrev_b32_e32 v92, 16, v116
	v_and_b32_e32 v93, s89, v116
	v_mul_f32_e32 v92, v92, v86
	v_mul_f32_e32 v93, v93, v87
	ds_write_b64 v83, v[92:93] offset:33280
	v_lshlrev_b32_e32 v92, 16, v101
	v_and_b32_e32 v93, s89, v101
	v_fmac_f32_e32 v84, 0x3fb8aa3b, v92
	v_fmac_f32_e32 v85, 0x3fb8aa3b, v93
	v_lshlrev_b32_e32 v94, 16, v105
	v_and_b32_e32 v95, s89, v105
	v_mul_f32_e32 v94, v94, v86
	v_mul_f32_e32 v95, v95, v87
	ds_write_b64 v83, v[94:95] offset:768
	v_exp_f32_e64 v88, -v84
	v_exp_f32_e64 v89, -v85
	v_exp_f32_e32 v90, v84
	v_exp_f32_e32 v91, v85
	v_lshlrev_b32_e32 v92, 16, v109
	v_and_b32_e32 v93, s89, v109
	v_mul_f32_e32 v92, v92, v90
	v_mul_f32_e32 v93, v93, v91
	ds_write_b64 v83, v[92:93] offset:8960
	ds_write_b64 v83, v[88:89] offset:17152
	v_lshlrev_b32_e32 v94, 16, v113
	v_and_b32_e32 v95, s89, v113
	v_mul_f32_e32 v94, v94, v90
	v_mul_f32_e32 v95, v95, v91
	ds_write_b64 v83, v[94:95] offset:25344
	v_lshlrev_b32_e32 v92, 16, v117
	v_and_b32_e32 v93, s89, v117
	ds_write_b64 v83, v[92:93] offset:33536
	s_mov_b32 s88, 0x15000
	s_mov_b32 s86, 0
	s_mov_b32 s7, 0
	s_mov_b32 s51, 0
	s_waitcnt lgkmcnt(0)
	s_barrier
.Lld_loop:
	s_cmp_eq_u32 s51, 0
	s_cbranch_scc1 .Lld_nost_a
	s_add_i32 s8, s86, -2
	s_lshl_b32 s8, s8, 2
	s_add_i32 s8, s8, s81
	s_mul_i32 s8, s8, s79
	s_add_i32 s8, s8, s2
	s_load_dwordx4 s[44:47], s[58:59], 0x268
	s_lshr_b32 s9, s8, 13
	s_bfe_u32 s33, s8, 0x40009
	s_and_b32 s48, s8, 31
	s_lshl_b32 s48, s48, 5
	s_bfe_u32 s49, s8, 0x40005
	s_lshl_b32 s49, s49, 7
	s_lshr_b32 s0, s48, 7
	s_lshl_b32 s0, s0, 8
	s_and_b32 s1, s48, 127
	s_add_i32 s0, s0, s1
	s_cmp_eq_u32 s9, 1
	s_cselect_b32 s1, 128, 0
	s_add_i32 s0, s0, s1
	s_cmp_lt_u32 s9, 2
	s_cselect_b32 s0, s0, s48
	s_cselect_b32 s1, 22, 21
	s_lshl_b32 s0, s0, 11
	s_add_i32 s0, s0, s49
	s_lshl_b32 s33, s33, s1
	s_add_i32 s0, s0, s33
	s_waitcnt lgkmcnt(0)
	s_cmp_lt_u32 s9, 2
	s_cselect_b32 s44, s44, s46
	s_cselect_b32 s45, s45, s47
	s_add_u32 s44, s44, s0
	s_addc_u32 s45, s45, 0
	s_add_u32 s46, s44, 0x1000
	s_addc_u32 s47, s45, 0
	v_cvt_pk_bf16_f32 v88, v50, v54
	v_cvt_pk_bf16_f32 v89, v58, v62
	v_cvt_pk_bf16_f32 v90, v66, v70
	v_cvt_pk_bf16_f32 v91, v74, v78
	global_store_dwordx4 v82, v[88:91], s[44:45]
	v_cvt_pk_bf16_f32 v92, v51, v55
	v_cvt_pk_bf16_f32 v93, v59, v63
	v_cvt_pk_bf16_f32 v94, v67, v71
	v_cvt_pk_bf16_f32 v95, v75, v79
	global_store_dwordx4 v82, v[92:95], s[44:45] offset:2048
	v_cvt_pk_bf16_f32 v88, v52, v56
	v_cvt_pk_bf16_f32 v89, v60, v64
	v_cvt_pk_bf16_f32 v90, v68, v72
	v_cvt_pk_bf16_f32 v91, v76, v80
	global_store_dwordx4 v82, v[88:91], s[46:47]
	v_cvt_pk_bf16_f32 v92, v53, v57
	v_cvt_pk_bf16_f32 v93, v61, v65
	v_cvt_pk_bf16_f32 v94, v69, v73
	v_cvt_pk_bf16_f32 v95, v77, v81
	global_store_dwordx4 v82, v[92:95], s[46:47] offset:2048

.Lld_ldone_a:
	s_cmp_eq_u32 s52, 0
	s_cbranch_scc1 .Lld_wA_a
	s_cmp_eq_u32 s51, 0
	s_cbranch_scc1 .Lld_wB_a
	s_waitcnt vmcnt(33)
	s_branch .Lld_proc_a
.Lld_wB_a:
	s_waitcnt vmcnt(29)
	s_branch .Lld_proc_a
.Lld_wA_a:
	s_cmp_eq_u32 s51, 0
	s_cbranch_scc1 .Lld_wC_a
	s_waitcnt vmcnt(25)
	s_branch .Lld_proc_a

.Lld_noproc_a:
	s_mov_b32 s51, s7
	s_mov_b32 s7, s52
	s_add_i32 s88, s88, 0xa800
	s_cmp_eq_u32 s88, 0x1f800
	s_cselect_b32 s88, 0, s88
	s_add_i32 s86, s86, 1
	s_waitcnt lgkmcnt(0)
	s_barrier
	s_cmp_eq_u32 s51, 0
	s_cbranch_scc1 .Lld_nost_b
	s_add_i32 s8, s86, -2
	s_lshl_b32 s8, s8, 2
	s_add_i32 s8, s8, s81
	s_mul_i32 s8, s8, s79
	s_add_i32 s8, s8, s2
	s_load_dwordx4 s[44:47], s[58:59], 0x268
	s_lshr_b32 s9, s8, 13
	s_bfe_u32 s33, s8, 0x40009
	s_and_b32 s48, s8, 31
	s_lshl_b32 s48, s48, 5
	s_bfe_u32 s49, s8, 0x40005
	s_lshl_b32 s49, s49, 7
	s_lshr_b32 s0, s48, 7
	s_lshl_b32 s0, s0, 8
	s_and_b32 s1, s48, 127
	s_add_i32 s0, s0, s1
	s_cmp_eq_u32 s9, 1
	s_cselect_b32 s1, 128, 0
	s_add_i32 s0, s0, s1
	s_cmp_lt_u32 s9, 2
	s_cselect_b32 s0, s0, s48
	s_cselect_b32 s1, 22, 21
	s_lshl_b32 s0, s0, 11
	s_add_i32 s0, s0, s49
	s_lshl_b32 s33, s33, s1
	s_add_i32 s0, s0, s33
	s_waitcnt lgkmcnt(0)
	s_cmp_lt_u32 s9, 2
	s_cselect_b32 s44, s44, s46
	s_cselect_b32 s45, s45, s47
	s_add_u32 s44, s44, s0
	s_addc_u32 s45, s45, 0
	s_add_u32 s46, s44, 0x1000
	s_addc_u32 s47, s45, 0
	v_cvt_pk_bf16_f32 v88, v30, v34
	v_cvt_pk_bf16_f32 v89, v38, v42
	v_cvt_pk_bf16_f32 v90, v46, v120
	v_cvt_pk_bf16_f32 v91, v124, v128
	global_store_dwordx4 v82, v[88:91], s[44:45]
	v_cvt_pk_bf16_f32 v92, v31, v35
	v_cvt_pk_bf16_f32 v93, v39, v43
	v_cvt_pk_bf16_f32 v94, v47, v121
	v_cvt_pk_bf16_f32 v95, v125, v129
	global_store_dwordx4 v82, v[92:95], s[44:45] offset:2048
	v_cvt_pk_bf16_f32 v88, v32, v36
	v_cvt_pk_bf16_f32 v89, v40, v44
	v_cvt_pk_bf16_f32 v90, v48, v122
	v_cvt_pk_bf16_f32 v91, v126, v130
	global_store_dwordx4 v82, v[88:91], s[46:47]
	v_cvt_pk_bf16_f32 v92, v33, v37
	v_cvt_pk_bf16_f32 v93, v41, v45
	v_cvt_pk_bf16_f32 v94, v49, v123
	v_cvt_pk_bf16_f32 v95, v127, v131
	global_store_dwordx4 v82, v[92:95], s[46:47] offset:2048
.Lld_nost_b:
	s_mov_b32 s52, 0
	s_lshl_b32 s8, s86, 2
	s_add_i32 s8, s8, s81
	s_mul_i32 s8, s8, s79
	s_add_i32 s8, s8, s2
	s_cmp_lg_u32 s57, s2
	s_cbranch_scc1 .Lld_nocvt_b
	s_cmp_lt_u32 s8, 0x6000
	s_cbranch_scc0 .Lld_nocvt_b
	s_mov_b32 s52, 1
	s_lshr_b32 s9, s8, 13
	s_lshl_b32 s9, s9, 3
	s_add_i32 s9, s9, 0xf8
	s_load_dwordx2 s[44:45], s[58:59], s9
	s_bfe_u32 s9, s8, 0x40009
	s_lshl_b32 s9, s9, 22
	s_bfe_u32 s33, s8, 0x40005
	s_lshl_b32 s33, s33, 18
	s_add_i32 s9, s9, s33
	s_and_b32 s33, s8, 31
	s_lshl_b32 s33, s33, 7
	s_add_i32 s9, s9, s33
	s_waitcnt lgkmcnt(0)
	s_add_u32 s44, s44, s68
	s_addc_u32 s45, s45, s69
	s_add_u32 s44, s44, s9
	s_addc_u32 s45, s45, 0
	global_load_dwordx4 v[30:33], v97, s[44:45] nt
	s_add_u32 s44, s44, 0x1000
	s_addc_u32 s45, s45, 0
	global_load_dwordx4 v[34:37], v97, s[44:45] nt
	s_add_u32 s44, s44, 0x1000
	s_addc_u32 s45, s45, 0
	global_load_dwordx4 v[38:41], v97, s[44:45] nt
	s_add_u32 s44, s44, 0x1000
	s_addc_u32 s45, s45, 0
	global_load_dwordx4 v[42:45], v97, s[44:45] nt
	s_add_u32 s44, s44, 0x1000
	s_addc_u32 s45, s45, 0
	global_load_dwordx4 v[46:49], v97, s[44:45] nt
	s_add_u32 s44, s44, 0x1000
	s_addc_u32 s45, s45, 0
	global_load_dwordx4 v[120:123], v97, s[44:45] nt
	s_add_u32 s44, s44, 0x1000
	s_addc_u32 s45, s45, 0
	global_load_dwordx4 v[124:127], v97, s[44:45] nt
	s_add_u32 s44, s44, 0x1000
	s_addc_u32 s45, s45, 0
	global_load_dwordx4 v[128:131], v97, s[44:45] nt

.Lld_noproc_b:
	s_mov_b32 s51, s7
	s_mov_b32 s7, s52
	s_add_i32 s88, s88, 0xa800
	s_cmp_eq_u32 s88, 0x1f800
	s_cselect_b32 s88, 0, s88
	s_add_i32 s86, s86, 1
	s_waitcnt lgkmcnt(0)
	s_barrier
	s_cmp_lt_u32 s86, 0x88
	s_cbranch_scc1 .Lld_loop
	s_branch .LBB0_602
